# attention K rows gathered by LDS-DMA straight into a per-wave swizzled 8 KB LDS tile (no ds_write), operand reads by ds_read_b128; DMA for the next step issued after the operand reads; even-step loads
# speedup vs baseline: 1.0168x; 1.0103x over previous
.LBB0_718:
	s_or_b64 exec, exec, s[12:13]
	s_cmp_eq_u32 s18, 2
	s_cselect_b32 s18, 32, 16
	s_lshl_b32 s12, s44, 9
	s_add_i32 s12, s12, 0
	v_lshlrev_b64 v[56:57], 1, v[14:15]
	v_lshl_add_u64 v[2:3], s[42:43], 0, v[56:57]
	s_waitcnt vmcnt(0)
	v_and_b32_e32 v200, 0x70, v52
	v_mov_b32_e32 v0, v200
	v_lshl_add_u64 v[212:213], s[42:43], 0, v[0:1]
	s_mov_b64 s[100:101], s[42:43]
	v_lshrrev_b32_e32 v196, 1, v233
	v_and_b32_e32 v197, 7, v232
	v_xor_b32_e32 v196, v196, v197
	v_lshlrev_b32_e32 v196, 4, v196
	v_xor_b32_e32 v197, 64, v196
	s_lshl_b32 s13, s96, 12
	s_add_i32 s13, s13, 0x10000
	v_lshrrev_b32_e32 v198, 1, v232
	v_lshrrev_b32_e32 v199, 1, v233
	v_xor_b32_e32 v198, v198, v199
	v_lshlrev_b32_e32 v198, 4, v198
	v_lshl_add_u32 v198, v232, 7, v198
	v_add_u32_e32 v198, s13, v198
	v_xor_b32_e32 v199, 64, v198
	v_lshl_add_u32 v70, v233, 1, s12
	ds_read_u16 v46, v70 offset:32768
	ds_read_u16 v50, v70 offset:32784
	ds_read_u16 v62, v70 offset:32800
	ds_read_u16 v66, v70 offset:32816
	ds_read_u16 v71, v70 offset:32832
	ds_read_u16 v74, v70 offset:32848
	ds_read_u16 v78, v70 offset:32864
	ds_read_u16 v82, v70 offset:32880
	s_waitcnt lgkmcnt(7)
	v_lshl_add_u32 v14, v46, 9, v196
	v_lshlrev_b32_e32 v0, 9, v46
	v_lshl_add_u64 v[46:47], v[212:213], 0, v[0:1]
	s_waitcnt lgkmcnt(6)
	v_lshl_add_u32 v15, v50, 9, v197
	v_lshlrev_b32_e32 v0, 9, v50
	v_lshl_add_u64 v[50:51], v[212:213], 0, v[0:1]
	s_waitcnt lgkmcnt(5)
	v_lshl_add_u32 v16, v62, 9, v196
	v_lshlrev_b32_e32 v0, 9, v62
	v_lshl_add_u64 v[62:63], v[212:213], 0, v[0:1]
	s_waitcnt lgkmcnt(4)
	v_lshl_add_u32 v17, v66, 9, v197
	v_lshlrev_b32_e32 v0, 9, v66
	v_lshl_add_u64 v[66:67], v[212:213], 0, v[0:1]
	s_waitcnt lgkmcnt(3)
	v_lshl_add_u32 v18, v71, 9, v196
	v_lshlrev_b32_e32 v0, 9, v71
	v_lshl_add_u64 v[70:71], v[212:213], 0, v[0:1]
	s_waitcnt lgkmcnt(2)
	v_lshl_add_u32 v19, v74, 9, v197
	v_lshlrev_b32_e32 v0, 9, v74
	v_lshl_add_u64 v[74:75], v[212:213], 0, v[0:1]
	s_waitcnt lgkmcnt(1)
	v_lshl_add_u32 v20, v78, 9, v196
	v_lshlrev_b32_e32 v0, 9, v78
	v_lshl_add_u64 v[78:79], v[212:213], 0, v[0:1]
	s_waitcnt lgkmcnt(0)
	v_lshl_add_u32 v21, v82, 9, v197
	v_lshlrev_b32_e32 v0, 9, v82
	v_lshl_add_u64 v[82:83], v[212:213], 0, v[0:1]
	global_load_dwordx4 v[46:49], v[46:47], off offset:128
	s_nop 0
	global_load_dwordx4 v[50:53], v[50:51], off offset:128
	s_nop 0
	global_load_dwordx4 v[62:65], v[62:63], off offset:128
	s_nop 0
	global_load_dwordx4 v[66:69], v[66:67], off offset:128
	s_nop 0
	global_load_dwordx4 v[70:73], v[70:71], off offset:128
	s_nop 0
	global_load_dwordx4 v[74:77], v[74:75], off offset:128
	s_nop 0
	global_load_dwordx4 v[78:81], v[78:79], off offset:128
	s_nop 0
	global_load_dwordx4 v[82:85], v[82:83], off offset:128
	s_waitcnt lgkmcnt(0)
	s_lshl_b32 m0, s96, 12
	s_add_u32 m0, m0, 0x10000
	s_nop 0
	global_load_lds_dwordx4 v14, s[100:101]
	s_add_u32 m0, m0, 0x400
	s_nop 0
	global_load_lds_dwordx4 v15, s[100:101]
	s_add_u32 m0, m0, 0x400
	s_nop 0
	global_load_lds_dwordx4 v16, s[100:101]
	s_add_u32 m0, m0, 0x400
	s_nop 0
	global_load_lds_dwordx4 v17, s[100:101]
	s_add_u32 m0, m0, 0x7400
	s_nop 0
	global_load_lds_dwordx4 v18, s[100:101]
	s_add_u32 m0, m0, 0x400
	s_nop 0
	global_load_lds_dwordx4 v19, s[100:101]
	s_add_u32 m0, m0, 0x400
	s_nop 0
	global_load_lds_dwordx4 v20, s[100:101]
	s_add_u32 m0, m0, 0x400
	s_nop 0
	global_load_lds_dwordx4 v21, s[100:101]
	v_mov_b32_e32 v0, v200
	v_lshlrev_b32_e32 v5, 6, v5
	s_mov_b32 s47, 2
	v_lshlrev_b32_e32 v210, 2, v54
	v_lshlrev_b32_e32 v54, 4, v233
	v_and_b32_e32 v54, 0x60, v54
	v_xad_u32 v61, v54, v0, s82
	v_lshrrev_b32_e32 v54, 2, v232
	v_or_b32_e32 v54, v210, v54
	v_and_b32_e32 v55, 24, v55
	v_lshlrev_b32_e32 v58, 4, v54
	v_lshl_add_u32 v87, v54, 7, s82
	v_add_u32_e32 v54, 16, v54
	v_lshlrev_b32_e32 v59, 4, v54
	v_lshl_add_u32 v89, v54, 7, s82
	v_or_b32_e32 v92, 32, v55
	s_movk_i32 s12, 0x60
	v_or_b32_e32 v94, 64, v55
	v_lshl_add_u64 v[212:213], s[42:43], 0, v[0:1]
	v_lshlrev_b32_e32 v0, 1, v5
	v_lshlrev_b32_e32 v60, 7, v233
	v_and_b32_e32 v86, 0x60, v58
	v_and_b32_e32 v88, 0x60, v59
	v_lshlrev_b32_e32 v54, 6, v232
	v_add_u32_e32 v90, v87, v55
	v_add_u32_e32 v91, v89, v55
	v_bitop3_b32 v93, v58, v92, s12 bitop3:0x6c
	v_bitop3_b32 v92, v59, v92, s12 bitop3:0x6c
	v_bitop3_b32 v95, v58, v94, s12 bitop3:0x6c
	v_bitop3_b32 v94, v59, v94, s12 bitop3:0x6c
	v_bitop3_b32 v96, v58, v55, s12 bitop3:0x4e
	v_bitop3_b32 v55, v59, v55, s12 bitop3:0x4e
	v_lshl_add_u64 v[58:59], s[74:75], 0, v[0:1]
	v_mov_b32_e32 v244, 0
	v_ashrrev_i32_e32 v211, 31, v210
	v_lshl_add_u64 v[214:215], v[58:59], 0, v[56:57]
	v_mov_b32_e32 v202, 0xf149f2ca
	v_lshlrev_b32_e32 v216, 1, v54
	v_mov_b32_e32 v5, v4
	v_add_u32_e32 v235, v61, v60
	v_add_u32_e32 v236, v90, v86
	v_add_u32_e32 v237, v91, v88
	v_add_u32_e32 v238, v87, v93
	v_add_u32_e32 v239, v89, v92
	v_add_u32_e32 v240, v87, v95
	v_add_u32_e32 v241, v89, v94
	v_add_u32_e32 v242, v87, v96
	v_add_u32_e32 v243, v89, v55
	v_mov_b32_e32 v154, 0
	v_mov_b32_e32 v155, v244
	v_mov_b32_e32 v156, v244
	v_mov_b32_e32 v157, v244
	v_mov_b32_e32 v158, 0
	v_mov_b32_e32 v159, v244
	v_mov_b32_e32 v160, v244
	v_mov_b32_e32 v161, v244
	v_mov_b32_e32 v162, 0
	v_mov_b32_e32 v163, v244
	v_mov_b32_e32 v164, v244
	v_mov_b32_e32 v165, v244
	v_mov_b32_e32 v166, 0
	v_mov_b32_e32 v167, v244
	v_mov_b32_e32 v168, v244
	v_mov_b32_e32 v169, v244
	s_branch .LBB0_720

.LBB0_720:
	s_add_i32 s12, s47, -2
	s_lshr_b32 s42, s12, 2
	s_add_i32 s42, s42, s44
	s_and_b32 s34, s12, 2
	s_lshl_b32 s12, s42, 9
	s_add_i32 s43, s12, 0
	s_lshl_b32 s12, s34, 7
	s_add_i32 s43, s43, s12
	v_lshl_add_u32 v90, v233, 1, s43
	ds_read_u16 v102, v90 offset:32896
	ds_read_u16 v106, v90 offset:32912
	ds_read_u16 v110, v90 offset:32928
	ds_read_u16 v114, v90 offset:32944
	ds_read_u16 v86, v90 offset:32960
	ds_read_u16 v91, v90 offset:32976
	ds_read_u16 v94, v90 offset:32992
	ds_read_u16 v98, v90 offset:33008
	s_waitcnt lgkmcnt(7)
	v_lshl_add_u32 v118, v102, 9, v196
	v_lshlrev_b32_e32 v0, 9, v102
	v_lshl_add_u64 v[102:103], v[212:213], 0, v[0:1]
	s_waitcnt lgkmcnt(6)
	v_lshl_add_u32 v119, v106, 9, v197
	v_lshlrev_b32_e32 v0, 9, v106
	v_lshl_add_u64 v[106:107], v[212:213], 0, v[0:1]
	s_waitcnt lgkmcnt(5)
	v_lshl_add_u32 v120, v110, 9, v196
	v_lshlrev_b32_e32 v0, 9, v110
	v_lshl_add_u64 v[110:111], v[212:213], 0, v[0:1]
	s_waitcnt lgkmcnt(4)
	v_lshl_add_u32 v121, v114, 9, v197
	v_lshlrev_b32_e32 v0, 9, v114
	v_lshl_add_u64 v[114:115], v[212:213], 0, v[0:1]
	s_waitcnt lgkmcnt(3)
	v_lshl_add_u32 v122, v86, 9, v196
	v_lshlrev_b32_e32 v0, 9, v86
	v_lshl_add_u64 v[86:87], v[212:213], 0, v[0:1]
	s_waitcnt lgkmcnt(2)
	v_lshl_add_u32 v123, v91, 9, v197
	v_lshlrev_b32_e32 v0, 9, v91
	v_lshl_add_u64 v[90:91], v[212:213], 0, v[0:1]
	s_waitcnt lgkmcnt(1)
	v_lshl_add_u32 v124, v94, 9, v196
	v_lshlrev_b32_e32 v0, 9, v94
	v_lshl_add_u64 v[94:95], v[212:213], 0, v[0:1]
	s_waitcnt lgkmcnt(0)
	v_lshl_add_u32 v125, v98, 9, v197
	v_lshlrev_b32_e32 v0, 9, v98
	v_lshl_add_u64 v[98:99], v[212:213], 0, v[0:1]
	global_load_dwordx4 v[102:105], v[102:103], off offset:128
	s_nop 0
	global_load_dwordx4 v[106:109], v[106:107], off offset:128
	s_nop 0
	global_load_dwordx4 v[110:113], v[110:111], off offset:128
	s_nop 0
	global_load_dwordx4 v[114:117], v[114:115], off offset:128
	s_nop 0
	global_load_dwordx4 v[86:89], v[86:87], off offset:128
	s_nop 0
	global_load_dwordx4 v[90:93], v[90:91], off offset:128
	s_nop 0
	global_load_dwordx4 v[94:97], v[94:95], off offset:128
	s_nop 0
	global_load_dwordx4 v[98:101], v[98:99], off offset:128
	s_cmp_eq_u32 s34, 0
	s_cselect_b64 s[30:31], -1, 0
	s_cmp_lg_u32 s34, 0
	s_cbranch_scc1 .LBB0_722
	v_mov_b32_e32 v244, 0
	v_mov_b32_e32 v202, 0xf149f2ca
	v_mov_b32_e32 v154, 0
	v_mov_b32_e32 v155, v244
	v_mov_b32_e32 v156, v244
	v_mov_b32_e32 v157, v244
	v_mov_b32_e32 v158, 0
	v_mov_b32_e32 v159, v244
	v_mov_b32_e32 v160, v244
	v_mov_b32_e32 v161, v244
	v_mov_b32_e32 v162, 0
	v_mov_b32_e32 v163, v244
	v_mov_b32_e32 v164, v244
	v_mov_b32_e32 v165, v244
	v_mov_b32_e32 v166, 0
	v_mov_b32_e32 v167, v244
	v_mov_b32_e32 v168, v244
	v_mov_b32_e32 v169, v244

.LBB0_736:
	s_waitcnt vmcnt(8)
	ds_read_b128 v[14:17], v198
	ds_read_b128 v[18:21], v199
	ds_read_b128 v[22:25], v198 offset:2048
	ds_read_b128 v[26:29], v199 offset:2048
	ds_read_b128 v[30:33], v198 offset:32768
	ds_read_b128 v[34:37], v199 offset:32768
	ds_read_b128 v[38:41], v198 offset:34816
	ds_read_b128 v[42:45], v199 offset:34816
	s_waitcnt lgkmcnt(0)
	s_lshl_b32 m0, s96, 12
	s_add_u32 m0, m0, 0x10000
	s_nop 0
	global_load_lds_dwordx4 v118, s[100:101]
	s_add_u32 m0, m0, 0x400
	s_nop 0
	global_load_lds_dwordx4 v119, s[100:101]
	s_add_u32 m0, m0, 0x400
	s_nop 0
	global_load_lds_dwordx4 v120, s[100:101]
	s_add_u32 m0, m0, 0x400
	s_nop 0
	global_load_lds_dwordx4 v121, s[100:101]
	s_add_u32 m0, m0, 0x7400
	s_nop 0
	global_load_lds_dwordx4 v122, s[100:101]
	s_add_u32 m0, m0, 0x400
	s_nop 0
	global_load_lds_dwordx4 v123, s[100:101]
	s_add_u32 m0, m0, 0x400
	s_nop 0
	global_load_lds_dwordx4 v124, s[100:101]
	s_add_u32 m0, m0, 0x400
	s_nop 0
	global_load_lds_dwordx4 v125, s[100:101]
	s_waitcnt vmcnt(31)
	v_mfma_f32_16x16x32_bf16 v[170:173], v[14:17], v[6:9], v[170:173]
	s_mov_b32 s12, 0x40c00000
	s_waitcnt vmcnt(30)
	v_mfma_f32_16x16x32_bf16 v[182:185], v[18:21], v[10:13], v[170:173]
	s_waitcnt vmcnt(29)
	v_mfma_f32_16x16x32_bf16 v[170:173], v[22:25], v[6:9], v[174:177]
	s_waitcnt vmcnt(28)
	v_mfma_f32_16x16x32_bf16 v[178:181], v[26:29], v[10:13], v[170:173]
	s_nop 3
	v_max_f32_e32 v0, v185, v185
	v_max_f32_e32 v153, v184, v184
	v_max_f32_e32 v0, v153, v0
	s_waitcnt vmcnt(27)
	v_mfma_f32_16x16x32_bf16 v[170:173], v[30:33], v[6:9], v[186:189]
	v_max3_f32 v0, v182, v183, v0
	v_max_f32_e32 v153, v181, v181
	s_waitcnt vmcnt(26)
	v_mfma_f32_16x16x32_bf16 v[174:177], v[34:37], v[10:13], v[170:173]
	v_max_f32_e32 v186, v180, v180
	v_max_f32_e32 v153, v186, v153
	v_max3_f32 v153, v178, v179, v153
	s_waitcnt vmcnt(25) lgkmcnt(0)
	v_mfma_f32_16x16x32_bf16 v[170:173], v[38:41], v[6:9], v[190:193]
	s_waitcnt vmcnt(24)
	v_mfma_f32_16x16x32_bf16 v[170:173], v[42:45], v[10:13], v[170:173]
	s_nop 0
	v_max_f32_e32 v186, v175, v175
	v_max_f32_e32 v187, v174, v174
	v_max_f32_e32 v186, v187, v186
	v_max_f32_e32 v187, v177, v177
	v_max_f32_e32 v188, v176, v176
	v_max_f32_e32 v187, v188, v187
	s_nop 0
	v_max_f32_e32 v188, v173, v173
	v_max_f32_e32 v189, v172, v172
	v_max_f32_e32 v188, v189, v188
	v_max3_f32 v188, v170, v171, v188
	v_max3_f32 v186, v186, v187, v188
	v_max3_f32 v0, v0, v153, v186
	v_mov_b32_e32 v153, v0
	s_nop 1
	v_permlane16_swap_b32_e32 v0, v153
	v_max_f32_e32 v153, v153, v153
	v_max_f32_e32 v0, v0, v0
	v_max_f32_e32 v0, v0, v153
	v_mov_b32_e32 v153, v0
	s_nop 1
	v_permlane32_swap_b32_e32 v0, v153
	v_max_f32_e32 v153, v153, v153
	v_max_f32_e32 v0, v0, v0
	v_max_f32_e32 v0, v0, v153
	v_sub_f32_e32 v153, v0, v202
	v_mul_f32_e32 v153, 0x3e38aa3b, v153
	v_cmp_lt_f32_e32 vcc, s12, v153
	s_cbranch_vccz .LBB0_738
	v_max_f32_e32 v0, v0, v0
	v_max_f32_e32 v153, v202, v202
	v_max_f32_e32 v153, v153, v0
	v_sub_f32_e32 v0, v202, v153
	v_mul_f32_e32 v0, 0x3e38aa3b, v0
	v_exp_f32_e32 v0, v0
	v_mov_b32_e32 v202, v153
	v_pk_mul_f32 v[168:169], v[168:169], v[0:1] op_sel_hi:[1,0]
	v_pk_mul_f32 v[166:167], v[166:167], v[0:1] op_sel_hi:[1,0]
	v_pk_mul_f32 v[164:165], v[164:165], v[0:1] op_sel_hi:[1,0]
	v_pk_mul_f32 v[162:163], v[162:163], v[0:1] op_sel_hi:[1,0]
	v_pk_mul_f32 v[160:161], v[160:161], v[0:1] op_sel_hi:[1,0]
	v_pk_mul_f32 v[158:159], v[158:159], v[0:1] op_sel_hi:[1,0]
	v_pk_mul_f32 v[156:157], v[156:157], v[0:1] op_sel_hi:[1,0]
	v_pk_mul_f32 v[154:155], v[154:155], v[0:1] op_sel_hi:[1,0]
	v_mul_f32_e32 v244, v244, v0

.Lattn_blkA_a:
	v_lshl_add_u32 v70, v233, 1, s12
	ds_read_u16 v46, v70 offset:32768
	ds_read_u16 v50, v70 offset:32784
	ds_read_u16 v62, v70 offset:32800
	ds_read_u16 v66, v70 offset:32816
	ds_read_u16 v71, v70 offset:32832
	ds_read_u16 v74, v70 offset:32848
	ds_read_u16 v78, v70 offset:32864
	ds_read_u16 v82, v70 offset:32880
	s_waitcnt lgkmcnt(7)
	v_lshl_add_u32 v14, v46, 9, v196
	v_lshlrev_b32_e32 v0, 9, v46
	v_lshl_add_u64 v[46:47], v[212:213], 0, v[0:1]
	s_waitcnt lgkmcnt(6)
	v_lshl_add_u32 v15, v50, 9, v197
	v_lshlrev_b32_e32 v0, 9, v50
	v_lshl_add_u64 v[50:51], v[212:213], 0, v[0:1]
	s_waitcnt lgkmcnt(5)
	v_lshl_add_u32 v16, v62, 9, v196
	v_lshlrev_b32_e32 v0, 9, v62
	v_lshl_add_u64 v[62:63], v[212:213], 0, v[0:1]
	s_waitcnt lgkmcnt(4)
	v_lshl_add_u32 v17, v66, 9, v197
	v_lshlrev_b32_e32 v0, 9, v66
	v_lshl_add_u64 v[66:67], v[212:213], 0, v[0:1]
	s_waitcnt lgkmcnt(3)
	v_lshl_add_u32 v18, v71, 9, v196
	v_lshlrev_b32_e32 v0, 9, v71
	v_lshl_add_u64 v[70:71], v[212:213], 0, v[0:1]
	s_waitcnt lgkmcnt(2)
	v_lshl_add_u32 v19, v74, 9, v197
	v_lshlrev_b32_e32 v0, 9, v74
	v_lshl_add_u64 v[74:75], v[212:213], 0, v[0:1]
	s_waitcnt lgkmcnt(1)
	v_lshl_add_u32 v20, v78, 9, v196
	v_lshlrev_b32_e32 v0, 9, v78
	v_lshl_add_u64 v[78:79], v[212:213], 0, v[0:1]
	s_waitcnt lgkmcnt(0)
	v_lshl_add_u32 v21, v82, 9, v197
	v_lshlrev_b32_e32 v0, 9, v82
	v_lshl_add_u64 v[82:83], v[212:213], 0, v[0:1]
	global_load_dwordx4 v[46:49], v[46:47], off offset:128
	s_nop 0
	global_load_dwordx4 v[50:53], v[50:51], off offset:128
	s_nop 0
	global_load_dwordx4 v[62:65], v[62:63], off offset:128
	s_nop 0
	global_load_dwordx4 v[66:69], v[66:67], off offset:128
	s_nop 0
	global_load_dwordx4 v[70:73], v[70:71], off offset:128
	s_nop 0
	global_load_dwordx4 v[74:77], v[74:75], off offset:128
	s_nop 0
	global_load_dwordx4 v[78:81], v[78:79], off offset:128
	s_nop 0
	global_load_dwordx4 v[82:85], v[82:83], off offset:128

.LBB0_760:
	s_waitcnt vmcnt(8)
	ds_read_b128 v[138:141], v198
	ds_read_b128 v[142:145], v199
	ds_read_b128 v[146:149], v198 offset:2048
	ds_read_b128 v[134:137], v199 offset:2048
	ds_read_b128 v[130:133], v198 offset:32768
	ds_read_b128 v[126:129], v199 offset:32768
	ds_read_b128 v[122:125], v198 offset:34816
	ds_read_b128 v[118:121], v199 offset:34816
	s_waitcnt lgkmcnt(0)
	s_lshl_b32 m0, s96, 12
	s_add_u32 m0, m0, 0x10000
	s_nop 0
	global_load_lds_dwordx4 v14, s[100:101]
	s_add_u32 m0, m0, 0x400
	s_nop 0
	global_load_lds_dwordx4 v15, s[100:101]
	s_add_u32 m0, m0, 0x400
	s_nop 0
	global_load_lds_dwordx4 v16, s[100:101]
	s_add_u32 m0, m0, 0x400
	s_nop 0
	global_load_lds_dwordx4 v17, s[100:101]
	s_add_u32 m0, m0, 0x7400
	s_nop 0
	global_load_lds_dwordx4 v18, s[100:101]
	s_add_u32 m0, m0, 0x400
	s_nop 0
	global_load_lds_dwordx4 v19, s[100:101]
	s_add_u32 m0, m0, 0x400
	s_nop 0
	global_load_lds_dwordx4 v20, s[100:101]
	s_add_u32 m0, m0, 0x400
	s_nop 0
	global_load_lds_dwordx4 v21, s[100:101]
	s_waitcnt vmcnt(31)
	v_mfma_f32_16x16x32_bf16 v[138:141], v[138:141], v[6:9], v[150:153]
	v_add_f32_e32 v0, v182, v183
	s_mov_b32 s12, 0x40c00000
	s_waitcnt vmcnt(27)
	v_mfma_f32_16x16x32_bf16 v[130:133], v[130:133], v[6:9], v[174:177]
	s_waitcnt vmcnt(25) lgkmcnt(0)
	v_mfma_f32_16x16x32_bf16 v[122:125], v[122:125], v[6:9], v[178:181]
	v_mfma_f32_16x16x32_bf16 v[138:141], v[142:145], v[10:13], v[138:141]
	v_add_f32_e32 v142, v244, v0
	v_mfma_f32_16x16x32_bf16 v[144:147], v[146:149], v[6:9], v[170:173]
	v_mfma_f32_16x16x32_bf16 v[126:129], v[126:129], v[10:13], v[130:133]
	s_nop 4
	v_max_f32_e32 v0, v141, v141
	v_max_f32_e32 v143, v140, v140
	v_max_f32_e32 v0, v143, v0
	s_waitcnt vmcnt(24)
	v_mfma_f32_16x16x32_bf16 v[118:121], v[118:121], v[10:13], v[122:125]
	v_max3_f32 v0, v138, v139, v0
	v_max_f32_e32 v130, v127, v127
	v_max_f32_e32 v131, v126, v126
	v_mfma_f32_16x16x32_bf16 v[134:137], v[134:137], v[10:13], v[144:147]
	v_max_f32_e32 v130, v131, v130
	s_nop 2
	v_max_f32_e32 v122, v121, v121
	v_max_f32_e32 v123, v120, v120
	v_max_f32_e32 v131, v129, v129
	v_max_f32_e32 v132, v128, v128
	v_max_f32_e32 v143, v137, v137
	v_max_f32_e32 v144, v136, v136
	v_max_f32_e32 v122, v123, v122
	v_max_f32_e32 v143, v144, v143
	v_max_f32_e32 v131, v132, v131
	v_max3_f32 v122, v118, v119, v122
	v_max3_f32 v143, v134, v135, v143
	v_max3_f32 v122, v130, v131, v122
	v_max3_f32 v0, v0, v143, v122
	v_mov_b32_e32 v122, v0
	s_nop 1
	v_permlane16_swap_b32_e32 v0, v122
	v_max_f32_e32 v122, v122, v122
	v_max_f32_e32 v0, v0, v0
	v_max_f32_e32 v0, v0, v122
	v_mov_b32_e32 v122, v0
	s_nop 1
	v_permlane32_swap_b32_e32 v0, v122
	v_max_f32_e32 v122, v122, v122
	v_max_f32_e32 v0, v0, v0
	v_max_f32_e32 v0, v0, v122
	v_sub_f32_e32 v122, v0, v202
	v_mul_f32_e32 v122, 0x3e38aa3b, v122
	v_cmp_lt_f32_e32 vcc, s12, v122
	s_cbranch_vccz .LBB0_762
	v_max_f32_e32 v0, v0, v0
	v_max_f32_e32 v122, v202, v202
	v_max_f32_e32 v143, v122, v0
	v_sub_f32_e32 v0, v202, v143
	v_mul_f32_e32 v0, 0x3e38aa3b, v0
	v_exp_f32_e32 v202, v0
	s_nop 0
	v_pk_mul_f32 v[186:187], v[142:143], v[202:203]
	v_pk_mul_f32 v[156:157], v[156:157], v[202:203] op_sel_hi:[1,0]
	v_pk_mul_f32 v[154:155], v[154:155], v[202:203] op_sel_hi:[1,0]
	v_pk_mul_f32 v[160:161], v[160:161], v[202:203] op_sel_hi:[1,0]
	v_pk_mul_f32 v[158:159], v[158:159], v[202:203] op_sel_hi:[1,0]
	v_pk_mul_f32 v[164:165], v[164:165], v[202:203] op_sel_hi:[1,0]
	v_pk_mul_f32 v[162:163], v[162:163], v[202:203] op_sel_hi:[1,0]
	v_pk_mul_f32 v[168:169], v[168:169], v[202:203] op_sel_hi:[1,0]
	v_pk_mul_f32 v[166:167], v[166:167], v[202:203] op_sel_hi:[1,0]
	v_mov_b32_e32 v202, v143
	v_mov_b32_e32 v142, v186
